# baseline (speedup 1.0000x reference)
.LBB0_55:
	s_waitcnt lgkmcnt(14)
	v_mfma_f32_16x16x32_f16 v[102:105], v[30:33], v[82:85], 0
	s_mul_i32 s40, s3, 13
	s_add_i32 s6, s42, s40
	s_lshl_b32 s6, s6, 8
	s_waitcnt lgkmcnt(11)
	v_mfma_f32_16x16x32_f16 v[110:113], v[46:49], v[82:85], 0
	s_lshl_b32 s38, s33, 6
	s_or_b32 s6, s6, s38
	v_mul_u32_u24_e32 v186, 0x650, v206
	s_waitcnt lgkmcnt(7)
	v_mfma_f32_16x16x32_f16 v[162:165], v[54:57], v[82:85], 0
	v_cmp_eq_u32_e64 s[14:15], 0, v1
	s_waitcnt lgkmcnt(3)
	v_mfma_f32_16x16x32_f16 v[82:85], v[62:65], v[82:85], 0
	v_mfma_f32_16x16x32_f16 v[102:105], v[22:25], v[78:81], v[102:105]
	v_mfma_f32_16x16x32_f16 v[110:113], v[34:37], v[78:81], v[110:113]
	v_mfma_f32_16x16x32_f16 v[162:165], v[50:53], v[78:81], v[162:165]
	s_waitcnt lgkmcnt(2)
	v_mfma_f32_16x16x32_f16 v[78:81], v[58:61], v[78:81], v[82:85]
	v_mfma_f32_16x16x32_f16 v[82:85], v[18:21], v[74:77], v[102:105]
	v_mfma_f32_16x16x32_f16 v[102:105], v[26:29], v[74:77], v[110:113]
	v_mfma_f32_16x16x32_f16 v[110:113], v[38:41], v[74:77], v[162:165]
	s_waitcnt lgkmcnt(1)
	v_mfma_f32_16x16x32_f16 v[74:77], v[42:45], v[74:77], v[78:81]
	s_nop 0
	v_or_b32_e32 v162, s6, v1
	v_mfma_f32_16x16x32_f16 v[78:81], v[14:17], v[70:73], v[82:85]
	v_mfma_f32_16x16x32_f16 v[82:85], v[2:5], v[70:73], v[102:105]
	v_mfma_f32_16x16x32_f16 v[102:105], v[6:9], v[70:73], v[110:113]
	s_nop 5
	v_max_f32_e32 v89, v79, v79
	v_max_f32_e32 v163, v78, v78
	v_max_f32_e32 v89, v163, v89
	v_max3_f32 v89, v89, v80, v81
	v_max3_f32 v89, v89, v82, v83
	s_waitcnt lgkmcnt(0)
	v_mfma_f32_16x16x32_f16 v[70:73], v[10:13], v[70:73], v[74:77]
	v_max3_f32 v89, v89, v84, v85
	v_max3_f32 v89, v89, v102, v103
	v_max3_f32 v89, v89, v104, v105
	v_ashrrev_i32_e32 v163, 31, v162
	s_nop 3
	v_max3_f32 v74, v89, v70, v71
	v_max3_f32 v74, v74, v72, v73
	v_mov_b32_e32 v75, v74
	s_nop 1
	v_permlane16_swap_b32_e32 v74, v75
	v_max_f32_e32 v75, v75, v75
	v_max_f32_e32 v74, v74, v74
	v_max_f32_e32 v74, v74, v75
	v_mov_b32_e32 v75, v74
	s_nop 1
	v_permlane32_swap_b32_e32 v74, v75
	v_max_f32_e32 v75, v75, v75
	v_max_f32_e32 v74, v74, v74
	v_max_f32_e32 v74, v74, v75
	v_mul_f32_e32 v89, 0xbfb8aa3b, v74
	v_fmamk_f32 v74, v78, 0x3fb8aa3b, v89
	v_exp_f32_e32 v74, v74
	v_fmamk_f32 v75, v79, 0x3fb8aa3b, v89
	v_exp_f32_e32 v75, v75
	v_fmamk_f32 v76, v80, 0x3fb8aa3b, v89
	v_exp_f32_e32 v76, v76
	v_fmamk_f32 v77, v81, 0x3fb8aa3b, v89
	v_exp_f32_e32 v77, v77
	v_add_f32_e32 v78, 0, v74
	v_add_f32_e32 v78, v75, v78
	v_add_f32_e32 v78, v76, v78
	v_add_f32_e32 v110, v77, v78
	v_fmamk_f32 v78, v82, 0x3fb8aa3b, v89
	v_exp_f32_e32 v78, v78
	v_fmamk_f32 v79, v83, 0x3fb8aa3b, v89
	v_exp_f32_e32 v79, v79
	v_fmamk_f32 v80, v84, 0x3fb8aa3b, v89
	v_exp_f32_e32 v80, v80
	v_fmamk_f32 v81, v85, 0x3fb8aa3b, v89
	v_exp_f32_e32 v81, v81
	v_add_f32_e32 v82, v78, v110
	v_add_f32_e32 v82, v79, v82
	v_add_f32_e32 v82, v80, v82
	v_add_f32_e32 v110, v81, v82
	v_fmamk_f32 v82, v102, 0x3fb8aa3b, v89
	v_exp_f32_e32 v82, v82
	v_fmamk_f32 v83, v103, 0x3fb8aa3b, v89
	v_exp_f32_e32 v83, v83
	v_fmamk_f32 v84, v104, 0x3fb8aa3b, v89
	v_exp_f32_e32 v84, v84
	v_fmamk_f32 v85, v105, 0x3fb8aa3b, v89
	v_exp_f32_e32 v85, v85
	v_fmamk_f32 v70, v70, 0x3fb8aa3b, v89
	v_add_f32_e32 v102, v82, v110
	v_exp_f32_e32 v70, v70
	v_fmamk_f32 v71, v71, 0x3fb8aa3b, v89
	v_add_f32_e32 v102, v83, v102
	v_exp_f32_e32 v71, v71
	v_fmamk_f32 v72, v72, 0x3fb8aa3b, v89
	v_add_f32_e32 v102, v84, v102
	v_exp_f32_e32 v72, v72
	v_fmac_f32_e32 v89, 0x3fb8aa3b, v73
	v_add_f32_e32 v102, v85, v102
	v_exp_f32_e32 v73, v89
	v_add_f32_e32 v89, v70, v102
	v_add_f32_e32 v89, v71, v89
	v_add_f32_e32 v89, v72, v89
	v_add_f32_e32 v89, v73, v89
	v_mov_b32_e32 v102, v89
	s_nop 1
	v_permlane16_swap_b32_e32 v89, v102
	v_add_f32_e32 v89, v89, v102
	v_mov_b32_e32 v102, v89
	s_nop 1
	v_permlane32_swap_b32_e32 v89, v102
	v_add_f32_e32 v89, v89, v102
	v_rcp_f32_e32 v102, v89
	v_lshl_add_u64 v[104:105], v[162:163], 4, s[20:21]
	global_store_dwordx4 v[104:105], v[66:69], off sc0 sc1 nt
	s_nop 1
	v_pk_mul_f32 v[66:67], v[102:103], v[74:75] op_sel_hi:[0,1]
	v_pk_mul_f32 v[68:69], v[102:103], v[76:77] op_sel_hi:[0,1]
	v_cvt_pk_f16_f32 v66, v66, v67
	v_cvt_pk_f16_f32 v67, v68, v69
	v_lshl_add_u32 v74, v87, 3, v186
	ds_write_b64 v74, v[66:67]
	v_pk_mul_f32 v[66:67], v[102:103], v[78:79] op_sel_hi:[0,1]
	v_pk_mul_f32 v[68:69], v[102:103], v[80:81] op_sel_hi:[0,1]
	v_cvt_pk_f16_f32 v66, v66, v67
	v_cvt_pk_f16_f32 v67, v68, v69
	ds_write_b64 v74, v[66:67] offset:6464
	v_pk_mul_f32 v[66:67], v[102:103], v[82:83] op_sel_hi:[0,1]
	v_pk_mul_f32 v[68:69], v[102:103], v[84:85] op_sel_hi:[0,1]
	v_cvt_pk_f16_f32 v66, v66, v67
	v_cvt_pk_f16_f32 v67, v68, v69
	ds_write_b64 v74, v[66:67] offset:12928
	v_pk_mul_f32 v[66:67], v[102:103], v[70:71] op_sel_hi:[0,1]
	v_pk_mul_f32 v[68:69], v[102:103], v[72:73] op_sel_hi:[0,1]
	v_cvt_pk_f16_f32 v66, v66, v67
	v_cvt_pk_f16_f32 v67, v68, v69
	ds_write_b64 v74, v[66:67] offset:19392
	s_waitcnt lgkmcnt(0)
	s_and_saveexec_b64 s[6:7], s[14:15]
	s_lshl_b32 s25, s42, 2
	s_add_i32 s25, s25, 0x14a00
	v_mov_b32_e32 v66, 1
	v_mov_b32_e32 v67, s25
	ds_write_b32 v67, v66
	s_or_b64 exec, exec, s[6:7]
	s_waitcnt vmcnt(11)
	v_ashrrev_i32_e32 v89, 31, v88
	v_or_b32_e32 v82, 0xc0, v87
	v_lshlrev_b64 v[66:67], 9, v[88:89]
	v_min_u32_e32 v82, 0xc7, v82
	v_lshl_add_u64 v[66:67], s[12:13], 0, v[66:67]
	v_lshlrev_b32_e32 v180, 2, v205
	v_mov_b32_e32 v181, 0
	v_add_u32_e32 v82, s37, v82
	v_lshl_add_u64 v[78:79], v[66:67], 0, v[180:181]
	v_ashrrev_i32_e32 v83, 31, v82
	global_load_dwordx4 v[174:177], v[78:79], off
	global_load_dwordx4 v[170:173], v[78:79], off offset:64
	global_load_dwordx4 v[166:169], v[78:79], off offset:128
	global_load_dwordx4 v[162:165], v[78:79], off offset:192
	global_load_dwordx4 v[66:69], v[78:79], off offset:256
	global_load_dwordx4 v[70:73], v[78:79], off offset:320
	global_load_dwordx4 v[74:77], v[78:79], off offset:384
	s_nop 0
	global_load_dwordx4 v[78:81], v[78:79], off offset:448
	v_lshl_add_u64 v[82:83], v[82:83], 2, s[8:9]
	s_waitcnt vmcnt(18)
	v_ashrrev_i32_e32 v87, 31, v86
	global_load_dword v182, v[82:83], off
	v_lshlrev_b64 v[82:83], 9, v[86:87]
	v_lshl_add_u64 v[82:83], s[12:13], 0, v[82:83]
	v_lshl_add_u64 v[184:185], v[82:83], 0, v[180:181]
	global_load_dwordx4 v[110:113], v[184:185], off
	global_load_dwordx4 v[102:105], v[184:185], off offset:64
	global_load_dwordx4 v[86:89], v[184:185], off offset:128
	global_load_dwordx4 v[82:85], v[184:185], off offset:192
	v_cvt_pk_f16_f32 v142, v142, v143
	v_cvt_pk_f16_f32 v143, v144, v145
	v_cvt_pk_f16_f32 v144, v138, v139
	v_cvt_pk_f16_f32 v145, v140, v141
	v_cvt_pk_f16_f32 v134, v134, v135
	v_cvt_pk_f16_f32 v135, v136, v137
	v_cvt_pk_f16_f32 v136, v130, v131
	v_cvt_pk_f16_f32 v137, v132, v133
	v_cvt_pk_f16_f32 v122, v122, v123
	v_cvt_pk_f16_f32 v123, v124, v125
	v_cvt_pk_f16_f32 v124, v118, v119
	v_cvt_pk_f16_f32 v125, v120, v121
	v_cvt_pk_f16_f32 v118, v90, v91
	v_cvt_pk_f16_f32 v119, v92, v93
	v_cvt_pk_f16_f32 v120, v94, v95
	v_cvt_pk_f16_f32 v121, v96, v97
	v_cndmask_b32_e64 v90, 0, 1, s[10:11]
	v_cmp_ne_u32_e64 s[6:7], 1, v90
	v_mov_b64_e32 v[90:91], v[142:143]
	s_andn2_b64 vcc, exec, s[10:11]
	v_mov_b64_e32 v[92:93], v[144:145]
	s_cbranch_vccnz .LBB0_59
	s_cmp_eq_u32 s33, 1
	s_cselect_b64 vcc, -1, 0
	s_cmp_eq_u32 s33, 2
	s_cselect_b64 s[8:9], -1, 0
	v_cndmask_b32_e64 v90, v118, v122, s[8:9]
	v_cndmask_b32_e64 v91, v119, v123, s[8:9]
	v_cndmask_b32_e64 v92, v120, v124, s[8:9]
	v_cndmask_b32_e64 v93, v121, v125, s[8:9]
	v_cndmask_b32_e32 v93, v93, v137, vcc
	v_cndmask_b32_e32 v92, v92, v136, vcc
	v_cndmask_b32_e32 v91, v91, v135, vcc
	v_cndmask_b32_e32 v90, v90, v134, vcc
.LBB0_59:
	v_mfma_f32_16x16x32_f16 v[94:97], v[30:33], v[142:145], 0
	s_add_i32 s8, s24, s40
	s_lshl_b32 s8, s8, 8
	s_or_b32 s8, s8, s38
	v_mfma_f32_16x16x32_f16 v[130:133], v[46:49], v[142:145], 0
	v_mfma_f32_16x16x32_f16 v[94:97], v[22:25], v[134:137], v[94:97]
	v_mfma_f32_16x16x32_f16 v[138:141], v[54:57], v[142:145], 0
	v_mfma_f32_16x16x32_f16 v[130:133], v[34:37], v[134:137], v[130:133]
	v_mfma_f32_16x16x32_f16 v[142:145], v[62:65], v[142:145], 0
	v_mfma_f32_16x16x32_f16 v[94:97], v[18:21], v[122:125], v[94:97]
	v_mfma_f32_16x16x32_f16 v[138:141], v[50:53], v[134:137], v[138:141]
	v_mfma_f32_16x16x32_f16 v[130:133], v[26:29], v[122:125], v[130:133]
	v_mfma_f32_16x16x32_f16 v[134:137], v[58:61], v[134:137], v[142:145]
	v_mfma_f32_16x16x32_f16 v[94:97], v[14:17], v[118:121], v[94:97]
	s_nop 2
	v_or_b32_e32 v142, s8, v1
	v_mfma_f32_16x16x32_f16 v[138:141], v[38:41], v[122:125], v[138:141]
	v_mfma_f32_16x16x32_f16 v[130:133], v[2:5], v[118:121], v[130:133]
	v_mfma_f32_16x16x32_f16 v[122:125], v[42:45], v[122:125], v[134:137]
	s_nop 2
	v_max_f32_e32 v134, v95, v95
	v_max_f32_e32 v135, v94, v94
	v_max_f32_e32 v134, v135, v134
	v_max3_f32 v134, v134, v96, v97
	v_max3_f32 v143, v134, v130, v131
	v_mfma_f32_16x16x32_f16 v[134:137], v[6:9], v[118:121], v[138:141]
	v_mfma_f32_16x16x32_f16 v[118:121], v[10:13], v[118:121], v[122:125]
	s_nop 1
	v_max3_f32 v138, v143, v132, v133
	s_nop 3
	v_max3_f32 v138, v138, v134, v135
	v_max3_f32 v138, v138, v136, v137
	v_ashrrev_i32_e32 v143, 31, v142
	v_max3_f32 v122, v138, v118, v119
	v_max3_f32 v122, v122, v120, v121
	v_mov_b32_e32 v123, v122
	s_nop 1
	v_permlane16_swap_b32_e32 v122, v123
	v_max_f32_e32 v123, v123, v123
	v_max_f32_e32 v122, v122, v122
	v_max_f32_e32 v122, v122, v123
	v_mov_b32_e32 v123, v122
	s_nop 1
	v_permlane32_swap_b32_e32 v122, v123
	v_max_f32_e32 v123, v123, v123
	v_max_f32_e32 v122, v122, v122
	v_max_f32_e32 v122, v122, v123
	v_mul_f32_e32 v138, 0xbfb8aa3b, v122
	v_fmamk_f32 v94, v94, 0x3fb8aa3b, v138
	v_exp_f32_e32 v94, v94
	v_fmamk_f32 v95, v95, 0x3fb8aa3b, v138
	v_exp_f32_e32 v95, v95
	v_fmamk_f32 v96, v96, 0x3fb8aa3b, v138
	v_exp_f32_e32 v96, v96
	v_fmamk_f32 v97, v97, 0x3fb8aa3b, v138
	v_exp_f32_e32 v97, v97
	v_add_f32_e32 v122, 0, v94
	v_add_f32_e32 v122, v95, v122
	v_add_f32_e32 v122, v96, v122
	v_add_f32_e32 v139, v97, v122
	v_fmamk_f32 v122, v130, 0x3fb8aa3b, v138
	v_exp_f32_e32 v122, v122
	v_fmamk_f32 v123, v131, 0x3fb8aa3b, v138
	v_exp_f32_e32 v123, v123
	v_fmamk_f32 v124, v132, 0x3fb8aa3b, v138
	v_exp_f32_e32 v124, v124
	v_fmamk_f32 v125, v133, 0x3fb8aa3b, v138
	v_exp_f32_e32 v125, v125
	v_add_f32_e32 v130, v122, v139
	v_add_f32_e32 v130, v123, v130
	v_add_f32_e32 v130, v124, v130
	v_add_f32_e32 v139, v125, v130
	v_fmamk_f32 v130, v134, 0x3fb8aa3b, v138
	v_exp_f32_e32 v130, v130
	v_fmamk_f32 v131, v135, 0x3fb8aa3b, v138
	v_exp_f32_e32 v131, v131
	v_fmamk_f32 v132, v136, 0x3fb8aa3b, v138
	v_exp_f32_e32 v132, v132
	v_fmamk_f32 v133, v137, 0x3fb8aa3b, v138
	v_exp_f32_e32 v133, v133
	v_fmamk_f32 v118, v118, 0x3fb8aa3b, v138
	v_add_f32_e32 v134, v130, v139
	v_exp_f32_e32 v118, v118
	v_fmamk_f32 v119, v119, 0x3fb8aa3b, v138
	v_add_f32_e32 v134, v131, v134
	v_exp_f32_e32 v119, v119
	v_fmamk_f32 v120, v120, 0x3fb8aa3b, v138
	v_add_f32_e32 v134, v132, v134
	v_exp_f32_e32 v120, v120
	v_fmac_f32_e32 v138, 0x3fb8aa3b, v121
	v_add_f32_e32 v134, v133, v134
	v_exp_f32_e32 v121, v138
	v_add_f32_e32 v134, v118, v134
	v_add_f32_e32 v134, v119, v134
	v_add_f32_e32 v134, v120, v134
	v_add_f32_e32 v134, v121, v134
	v_mov_b32_e32 v135, v134
	s_nop 1
	v_permlane16_swap_b32_e32 v134, v135
	v_add_f32_e32 v134, v134, v135
	v_mov_b32_e32 v135, v134
	s_nop 1
	v_permlane32_swap_b32_e32 v134, v135
	v_add_f32_e32 v134, v134, v135
	v_rcp_f32_e32 v134, v134
	v_lshl_add_u64 v[136:137], v[142:143], 4, s[20:21]
	global_store_dwordx4 v[136:137], v[90:93], off sc0 sc1 nt
	s_nop 1
	v_pk_mul_f32 v[90:91], v[134:135], v[94:95] op_sel_hi:[0,1]
	v_pk_mul_f32 v[92:93], v[134:135], v[96:97] op_sel_hi:[0,1]
	v_cvt_pk_f16_f32 v90, v90, v91
	v_cvt_pk_f16_f32 v91, v92, v93
	v_lshl_add_u32 v94, v179, 3, v186
	ds_write_b64 v94, v[90:91]
	v_pk_mul_f32 v[90:91], v[134:135], v[122:123] op_sel_hi:[0,1]
	v_pk_mul_f32 v[92:93], v[134:135], v[124:125] op_sel_hi:[0,1]
	v_cvt_pk_f16_f32 v90, v90, v91
	v_cvt_pk_f16_f32 v91, v92, v93
	ds_write_b64 v94, v[90:91] offset:6464
	v_pk_mul_f32 v[90:91], v[134:135], v[130:131] op_sel_hi:[0,1]
	v_pk_mul_f32 v[92:93], v[134:135], v[132:133] op_sel_hi:[0,1]
	v_cvt_pk_f16_f32 v90, v90, v91
	v_cvt_pk_f16_f32 v91, v92, v93
	ds_write_b64 v94, v[90:91] offset:12928
	v_pk_mul_f32 v[90:91], v[134:135], v[118:119] op_sel_hi:[0,1]
	v_pk_mul_f32 v[92:93], v[134:135], v[120:121] op_sel_hi:[0,1]
	v_cvt_pk_f16_f32 v90, v90, v91
	v_cvt_pk_f16_f32 v91, v92, v93
	ds_write_b64 v94, v[90:91] offset:19392
	s_waitcnt lgkmcnt(0)
	s_and_saveexec_b64 s[8:9], s[14:15]
	s_lshl_b32 s10, s24, 2
	s_add_i32 s10, s10, 0x14a00
	v_mov_b32_e32 v90, 1
	v_mov_b32_e32 v91, s10
	ds_write_b32 v91, v90
	s_or_b64 exec, exec, s[8:9]
	s_waitcnt vmcnt(15)
	v_ashrrev_i32_e32 v179, 31, v178
	v_lshlrev_b64 v[90:91], 9, v[178:179]
	v_lshl_add_u64 v[90:91], s[12:13], 0, v[90:91]
	v_mov_b32_e32 v181, 0
	v_lshl_add_u64 v[178:179], v[90:91], 0, v[180:181]
	global_load_dwordx4 v[142:145], v[184:185], off offset:256
	global_load_dwordx4 v[138:141], v[184:185], off offset:320
	global_load_dwordx4 v[134:137], v[184:185], off offset:384
	global_load_dwordx4 v[130:133], v[184:185], off offset:448
	global_load_dwordx4 v[122:125], v[178:179], off
	global_load_dwordx4 v[118:121], v[178:179], off offset:64
	global_load_dwordx4 v[94:97], v[178:179], off offset:128
	global_load_dwordx4 v[90:93], v[178:179], off offset:192
	v_cvt_pk_f16_f32 v158, v158, v159
	v_cvt_pk_f16_f32 v159, v160, v161
	v_cvt_pk_f16_f32 v160, v154, v155
	v_cvt_pk_f16_f32 v161, v156, v157
	v_cvt_pk_f16_f32 v150, v150, v151
	v_cvt_pk_f16_f32 v151, v152, v153
	v_cvt_pk_f16_f32 v152, v146, v147
	v_cvt_pk_f16_f32 v153, v148, v149
	v_cvt_pk_f16_f32 v126, v126, v127
	v_cvt_pk_f16_f32 v127, v128, v129
	v_cvt_pk_f16_f32 v128, v114, v115
	v_cvt_pk_f16_f32 v129, v116, v117
	v_cvt_pk_f16_f32 v106, v106, v107
	v_cvt_pk_f16_f32 v107, v108, v109
	v_cvt_pk_f16_f32 v108, v98, v99
	v_cvt_pk_f16_f32 v109, v100, v101
	v_mov_b64_e32 v[98:99], v[158:159]
	s_and_b64 vcc, exec, s[6:7]
	v_mov_b64_e32 v[100:101], v[160:161]
	s_cbranch_vccnz .LBB0_63
	s_cmp_eq_u32 s33, 1
	s_cselect_b64 vcc, -1, 0
	s_cmp_eq_u32 s33, 2
	s_cselect_b64 s[8:9], -1, 0
	v_cndmask_b32_e64 v98, v106, v126, s[8:9]
	v_cndmask_b32_e64 v99, v107, v127, s[8:9]
	v_cndmask_b32_e64 v100, v108, v128, s[8:9]
	v_cndmask_b32_e64 v101, v109, v129, s[8:9]
	v_cndmask_b32_e32 v101, v101, v153, vcc
	v_cndmask_b32_e32 v100, v100, v152, vcc
	v_cndmask_b32_e32 v99, v99, v151, vcc
	v_cndmask_b32_e32 v98, v98, v150, vcc
.LBB0_63:
	v_mfma_f32_16x16x32_f16 v[114:117], v[30:33], v[158:161], 0
	s_add_i32 s8, s36, s40
	s_lshl_b32 s8, s8, 8
	s_or_b32 s8, s8, s38
	v_mfma_f32_16x16x32_f16 v[146:149], v[46:49], v[158:161], 0
	v_mfma_f32_16x16x32_f16 v[114:117], v[22:25], v[150:153], v[114:117]
	v_mfma_f32_16x16x32_f16 v[154:157], v[54:57], v[158:161], 0
	v_mfma_f32_16x16x32_f16 v[146:149], v[34:37], v[150:153], v[146:149]
	v_mfma_f32_16x16x32_f16 v[158:161], v[62:65], v[158:161], 0
	v_mfma_f32_16x16x32_f16 v[114:117], v[18:21], v[126:129], v[114:117]
	v_mfma_f32_16x16x32_f16 v[154:157], v[50:53], v[150:153], v[154:157]
	v_mfma_f32_16x16x32_f16 v[146:149], v[26:29], v[126:129], v[146:149]
	v_mfma_f32_16x16x32_f16 v[150:153], v[58:61], v[150:153], v[158:161]
	v_mfma_f32_16x16x32_f16 v[114:117], v[14:17], v[106:109], v[114:117]
	s_nop 2
	v_or_b32_e32 v158, s8, v1
	v_mfma_f32_16x16x32_f16 v[154:157], v[38:41], v[126:129], v[154:157]
	v_mfma_f32_16x16x32_f16 v[146:149], v[2:5], v[106:109], v[146:149]
	v_mfma_f32_16x16x32_f16 v[126:129], v[42:45], v[126:129], v[150:153]
	s_nop 2
	v_max_f32_e32 v150, v115, v115
	v_max_f32_e32 v151, v114, v114
	v_max_f32_e32 v150, v151, v150
	v_max3_f32 v150, v150, v116, v117
	v_max3_f32 v159, v150, v146, v147
	v_mfma_f32_16x16x32_f16 v[150:153], v[6:9], v[106:109], v[154:157]
	v_mfma_f32_16x16x32_f16 v[106:109], v[10:13], v[106:109], v[126:129]
	s_nop 1
	v_max3_f32 v154, v159, v148, v149
	s_nop 3
	v_max3_f32 v154, v154, v150, v151
	v_max3_f32 v154, v154, v152, v153
	v_ashrrev_i32_e32 v159, 31, v158
	v_max3_f32 v126, v154, v106, v107
	v_max3_f32 v126, v126, v108, v109
	v_mov_b32_e32 v127, v126
	s_nop 1
	v_permlane16_swap_b32_e32 v126, v127
	v_max_f32_e32 v127, v127, v127
	v_max_f32_e32 v126, v126, v126
	v_max_f32_e32 v126, v126, v127
	v_mov_b32_e32 v127, v126
	s_nop 1
	v_permlane32_swap_b32_e32 v126, v127
	v_max_f32_e32 v127, v127, v127
	v_max_f32_e32 v126, v126, v126
	v_max_f32_e32 v126, v126, v127
	v_mul_f32_e32 v154, 0xbfb8aa3b, v126
	v_fmamk_f32 v114, v114, 0x3fb8aa3b, v154
	v_exp_f32_e32 v114, v114
	v_fmamk_f32 v115, v115, 0x3fb8aa3b, v154
	v_exp_f32_e32 v115, v115
	v_fmamk_f32 v116, v116, 0x3fb8aa3b, v154
	v_exp_f32_e32 v116, v116
	v_fmamk_f32 v117, v117, 0x3fb8aa3b, v154
	v_exp_f32_e32 v117, v117
	v_add_f32_e32 v126, 0, v114
	v_add_f32_e32 v126, v115, v126
	v_add_f32_e32 v126, v116, v126
	v_add_f32_e32 v155, v117, v126
	v_fmamk_f32 v126, v146, 0x3fb8aa3b, v154
	v_exp_f32_e32 v126, v126
	v_fmamk_f32 v127, v147, 0x3fb8aa3b, v154
	v_exp_f32_e32 v127, v127
	v_fmamk_f32 v128, v148, 0x3fb8aa3b, v154
	v_exp_f32_e32 v128, v128
	v_fmamk_f32 v129, v149, 0x3fb8aa3b, v154
	v_exp_f32_e32 v129, v129
	v_add_f32_e32 v146, v126, v155
	v_add_f32_e32 v146, v127, v146
	v_add_f32_e32 v146, v128, v146
	v_add_f32_e32 v155, v129, v146
	v_fmamk_f32 v146, v150, 0x3fb8aa3b, v154
	v_exp_f32_e32 v146, v146
	v_fmamk_f32 v147, v151, 0x3fb8aa3b, v154
	v_exp_f32_e32 v147, v147
	v_fmamk_f32 v148, v152, 0x3fb8aa3b, v154
	v_exp_f32_e32 v148, v148
	v_fmamk_f32 v149, v153, 0x3fb8aa3b, v154
	v_exp_f32_e32 v149, v149
	v_fmamk_f32 v106, v106, 0x3fb8aa3b, v154
	v_add_f32_e32 v150, v146, v155
	v_exp_f32_e32 v106, v106
	v_fmamk_f32 v107, v107, 0x3fb8aa3b, v154
	v_add_f32_e32 v150, v147, v150
	v_exp_f32_e32 v107, v107
	v_fmamk_f32 v108, v108, 0x3fb8aa3b, v154
	v_add_f32_e32 v150, v148, v150
	v_exp_f32_e32 v108, v108
	v_fmac_f32_e32 v154, 0x3fb8aa3b, v109
	v_add_f32_e32 v150, v149, v150
	v_exp_f32_e32 v109, v154
	v_add_f32_e32 v150, v106, v150
	v_add_f32_e32 v150, v107, v150
	v_add_f32_e32 v150, v108, v150
	v_add_f32_e32 v150, v109, v150
	v_mov_b32_e32 v151, v150
	s_nop 1
	v_permlane16_swap_b32_e32 v150, v151
	v_add_f32_e32 v150, v150, v151
	v_mov_b32_e32 v151, v150
	s_nop 1
	v_permlane32_swap_b32_e32 v150, v151
	v_add_f32_e32 v150, v150, v151
	v_rcp_f32_e32 v150, v150
	v_lshl_add_u64 v[152:153], v[158:159], 4, s[20:21]
	global_store_dwordx4 v[152:153], v[98:101], off sc0 sc1 nt
	s_nop 1
	v_pk_mul_f32 v[98:99], v[150:151], v[114:115] op_sel_hi:[0,1]
	v_pk_mul_f32 v[100:101], v[150:151], v[116:117] op_sel_hi:[0,1]
	v_cvt_pk_f16_f32 v98, v98, v99
	v_cvt_pk_f16_f32 v99, v100, v101
	v_lshl_add_u32 v114, v204, 3, v186
	ds_write_b64 v114, v[98:99]
	v_pk_mul_f32 v[98:99], v[150:151], v[126:127] op_sel_hi:[0,1]
	v_pk_mul_f32 v[100:101], v[150:151], v[128:129] op_sel_hi:[0,1]
	v_cvt_pk_f16_f32 v98, v98, v99
	v_cvt_pk_f16_f32 v99, v100, v101
	ds_write_b64 v114, v[98:99] offset:6464
	v_pk_mul_f32 v[98:99], v[150:151], v[146:147] op_sel_hi:[0,1]
	v_pk_mul_f32 v[100:101], v[150:151], v[148:149] op_sel_hi:[0,1]
	v_cvt_pk_f16_f32 v98, v98, v99
	v_cvt_pk_f16_f32 v99, v100, v101
	ds_write_b64 v114, v[98:99] offset:12928
	v_pk_mul_f32 v[98:99], v[150:151], v[106:107] op_sel_hi:[0,1]
	v_pk_mul_f32 v[100:101], v[150:151], v[108:109] op_sel_hi:[0,1]
	v_cvt_pk_f16_f32 v98, v98, v99
	v_cvt_pk_f16_f32 v99, v100, v101
	ds_write_b64 v114, v[98:99] offset:19392
	s_waitcnt lgkmcnt(0)
	s_and_saveexec_b64 s[8:9], s[14:15]
	s_lshl_b32 s10, s36, 2
	s_add_i32 s10, s10, 0x14a00
	v_mov_b32_e32 v98, 1
	v_mov_b32_e32 v99, s10
	ds_write_b32 v99, v98
	s_or_b64 exec, exec, s[8:9]
	global_load_dwordx4 v[158:161], v[178:179], off offset:256
	global_load_dwordx4 v[154:157], v[178:179], off offset:320
	global_load_dwordx4 v[150:153], v[178:179], off offset:384
	global_load_dwordx4 v[146:149], v[178:179], off offset:448
	v_mov_b32_e32 v181, 0
	s_waitcnt vmcnt(18)
	v_ashrrev_i32_e32 v183, 31, v182
	v_lshl_add_u64 v[98:99], s[12:13], 0, v[180:181]
	v_lshlrev_b64 v[100:101], 9, v[182:183]
	s_cmp_eq_u32 s42, 0
	v_lshl_add_u64 v[182:183], v[98:99], 0, v[100:101]
	s_cselect_b64 s[24:25], -1, 0
	s_cmp_lg_u32 s42, 0
	v_mov_b64_e32 v[98:99], v[174:175]
	v_mov_b64_e32 v[100:101], v[176:177]
	v_mov_b64_e32 v[106:107], v[170:171]
	v_mov_b64_e32 v[108:109], v[172:173]
	v_mov_b64_e32 v[114:115], v[166:167]
	v_mov_b64_e32 v[116:117], v[168:169]
	v_mov_b64_e32 v[126:127], v[162:163]
	v_mov_b64_e32 v[128:129], v[164:165]
	s_cbranch_scc1 .LBB0_67
	global_load_dwordx4 v[98:101], v[182:183], off
	global_load_dwordx4 v[106:109], v[182:183], off offset:64
	global_load_dwordx4 v[114:117], v[182:183], off offset:128
	global_load_dwordx4 v[126:129], v[182:183], off offset:192

.LBB0_69:
	v_mfma_f32_16x16x32_f16 v[188:191], v[30:33], v[174:177], 0
	s_add_i32 s12, s39, s40
	v_lshl_or_b32 v184, s12, 8, v1
	s_movk_i32 s12, 0xc8
	v_mfma_f32_16x16x32_f16 v[192:195], v[46:49], v[174:177], 0
	v_mfma_f32_16x16x32_f16 v[200:203], v[54:57], v[174:177], 0
	v_mfma_f32_16x16x32_f16 v[174:177], v[62:65], v[174:177], 0
	v_mfma_f32_16x16x32_f16 v[188:191], v[22:25], v[166:169], v[188:191]
	v_mfma_f32_16x16x32_f16 v[192:195], v[34:37], v[166:169], v[192:195]
	v_mfma_f32_16x16x32_f16 v[200:203], v[50:53], v[166:169], v[200:203]
	v_mfma_f32_16x16x32_f16 v[166:169], v[58:61], v[166:169], v[174:177]
	v_mfma_f32_16x16x32_f16 v[174:177], v[18:21], v[170:173], v[188:191]
	v_mfma_f32_16x16x32_f16 v[188:191], v[26:29], v[170:173], v[192:195]
	v_mfma_f32_16x16x32_f16 v[192:195], v[38:41], v[170:173], v[200:203]
	v_mfma_f32_16x16x32_f16 v[166:169], v[42:45], v[170:173], v[166:169]
	v_or_b32_e32 v170, s38, v184
	v_ashrrev_i32_e32 v171, 31, v170
	v_lshl_add_u64 v[184:185], v[170:171], 4, s[20:21]
	v_mfma_f32_16x16x32_f16 v[170:173], v[14:17], v[162:165], v[174:177]
	global_store_dwordx4 v[184:185], v[178:181], off sc0 sc1 nt
	v_mfma_f32_16x16x32_f16 v[174:177], v[2:5], v[162:165], v[188:191]
	v_mfma_f32_16x16x32_f16 v[188:191], v[10:13], v[162:165], v[166:169]
	s_nop 4
	v_max_f32_e32 v178, v171, v171
	v_max_f32_e32 v179, v170, v170
	v_max_f32_e32 v178, v179, v178
	v_max3_f32 v178, v178, v172, v173
	v_max3_f32 v184, v178, v174, v175
	v_mfma_f32_16x16x32_f16 v[178:181], v[6:9], v[162:165], v[192:195]
	v_max3_f32 v184, v184, v176, v177
	s_nop 6
	v_max3_f32 v184, v184, v178, v179
	v_max3_f32 v184, v184, v180, v181
	v_max3_f32 v162, v184, v188, v189
	v_max3_f32 v162, v162, v190, v191
	v_mov_b32_e32 v163, v162
	s_nop 1
	v_permlane16_swap_b32_e32 v162, v163
	v_max_f32_e32 v163, v163, v163
	v_max_f32_e32 v162, v162, v162
	v_max_f32_e32 v162, v162, v163
	v_mov_b32_e32 v163, v162
	s_nop 1
	v_permlane32_swap_b32_e32 v162, v163
	v_max_f32_e32 v163, v163, v163
	v_max_f32_e32 v162, v162, v162
	v_max_f32_e32 v162, v162, v163
	v_mul_f32_e32 v184, 0xbfb8aa3b, v162
	v_fmamk_f32 v162, v170, 0x3fb8aa3b, v184
	v_exp_f32_e32 v162, v162
	v_fmamk_f32 v163, v171, 0x3fb8aa3b, v184
	v_exp_f32_e32 v163, v163
	v_fmamk_f32 v164, v172, 0x3fb8aa3b, v184
	v_exp_f32_e32 v164, v164
	v_fmamk_f32 v165, v173, 0x3fb8aa3b, v184
	v_exp_f32_e32 v165, v165
	v_add_f32_e32 v166, 0, v162
	v_add_f32_e32 v166, v163, v166
	v_add_f32_e32 v166, v164, v166
	v_add_f32_e32 v170, v165, v166
	v_fmamk_f32 v166, v174, 0x3fb8aa3b, v184
	v_exp_f32_e32 v166, v166
	v_fmamk_f32 v167, v175, 0x3fb8aa3b, v184
	v_exp_f32_e32 v167, v167
	v_fmamk_f32 v168, v176, 0x3fb8aa3b, v184
	v_exp_f32_e32 v168, v168
	v_fmamk_f32 v169, v177, 0x3fb8aa3b, v184
	v_exp_f32_e32 v169, v169
	v_add_f32_e32 v170, v166, v170
	v_add_f32_e32 v170, v167, v170
	v_add_f32_e32 v170, v168, v170
	v_add_f32_e32 v174, v169, v170
	v_fmamk_f32 v170, v178, 0x3fb8aa3b, v184
	v_exp_f32_e32 v170, v170
	v_fmamk_f32 v171, v179, 0x3fb8aa3b, v184
	v_exp_f32_e32 v171, v171
	v_fmamk_f32 v172, v180, 0x3fb8aa3b, v184
	v_exp_f32_e32 v172, v172
	v_fmamk_f32 v173, v181, 0x3fb8aa3b, v184
	v_exp_f32_e32 v173, v173
	v_add_f32_e32 v174, v170, v174
	v_add_f32_e32 v174, v171, v174
	v_add_f32_e32 v174, v172, v174
	v_add_f32_e32 v178, v173, v174
	v_fmamk_f32 v174, v188, 0x3fb8aa3b, v184
	v_exp_f32_e32 v174, v174
	v_fmamk_f32 v175, v189, 0x3fb8aa3b, v184
	v_exp_f32_e32 v175, v175
	v_fmamk_f32 v176, v190, 0x3fb8aa3b, v184
	v_exp_f32_e32 v176, v176
	v_fmac_f32_e32 v184, 0x3fb8aa3b, v191
	v_exp_f32_e32 v177, v184
	v_add_f32_e32 v178, v174, v178
	v_add_f32_e32 v178, v175, v178
	v_add_f32_e32 v178, v176, v178
	v_add_f32_e32 v179, v177, v178
	v_mov_b32_e32 v180, v179
	s_nop 1
	v_permlane16_swap_b32_e32 v179, v180
	v_add_f32_e32 v179, v179, v180
	v_or_b32_e32 v178, s41, v199
	v_mov_b32_e32 v180, v179
	s_nop 1
	v_permlane32_swap_b32_e32 v179, v180
	v_cmp_gt_u32_e32 vcc, s12, v178
	s_and_saveexec_b64 s[12:13], vcc
	s_cbranch_execz .LBB0_71
	v_add_f32_e32 v179, v179, v180
	v_rcp_f32_e32 v180, v179
	v_lshl_add_u32 v178, v178, 3, v186
	v_pk_mul_f32 v[162:163], v[180:181], v[162:163] op_sel_hi:[0,1]
	v_pk_mul_f32 v[164:165], v[180:181], v[164:165] op_sel_hi:[0,1]
	v_cvt_pk_f16_f32 v162, v162, v163
	v_cvt_pk_f16_f32 v163, v164, v165
	ds_write_b64 v178, v[162:163]
	v_pk_mul_f32 v[162:163], v[180:181], v[166:167] op_sel_hi:[0,1]
	v_pk_mul_f32 v[164:165], v[180:181], v[168:169] op_sel_hi:[0,1]
	v_cvt_pk_f16_f32 v162, v162, v163
	v_cvt_pk_f16_f32 v163, v164, v165
	ds_write_b64 v178, v[162:163] offset:6464
	v_pk_mul_f32 v[162:163], v[180:181], v[170:171] op_sel_hi:[0,1]
	v_pk_mul_f32 v[164:165], v[180:181], v[172:173] op_sel_hi:[0,1]
	v_cvt_pk_f16_f32 v162, v162, v163
	v_cvt_pk_f16_f32 v163, v164, v165
	ds_write_b64 v178, v[162:163] offset:12928
	v_pk_mul_f32 v[162:163], v[180:181], v[174:175] op_sel_hi:[0,1]
	v_pk_mul_f32 v[164:165], v[180:181], v[176:177] op_sel_hi:[0,1]
	v_cvt_pk_f16_f32 v162, v162, v163
	v_cvt_pk_f16_f32 v163, v164, v165
	ds_write_b64 v178, v[162:163] offset:19392

.Lc0_fin2:
	ds_read_b128 v[112:115], v43 offset:2048
	ds_read_b128 v[116:119], v43 offset:3072
	s_waitcnt lgkmcnt(0)
	v_pk_add_f16 v112, v112, v116
	v_pk_add_f16 v113, v113, v117
	v_pk_add_f16 v114, v114, v118
	v_pk_add_f16 v115, v115, v119
	s_mov_b32 exec_lo, -1
	s_mov_b32 exec_hi, 0
	global_store_dwordx4 v35, v[112:115], s[68:69] sc0 sc1 nt

.Lc1_dback0:
	v_pk_add_f16 v112, v112, v116
	v_pk_add_f16 v113, v113, v117
	v_pk_add_f16 v114, v114, v118
	v_pk_add_f16 v115, v115, v119
	global_store_dwordx4 v35, v[112:115], s[68:69] offset:-1024 sc0 sc1 nt

.Lc1_dback1:
	v_pk_add_f16 v112, v112, v116
	v_pk_add_f16 v113, v113, v117
	v_pk_add_f16 v114, v114, v118
	v_pk_add_f16 v115, v115, v119
	global_store_dwordx4 v35, v[112:115], s[68:69] offset:0 sc0 sc1 nt

.LBB0_108:
	s_waitcnt vmcnt(18)
	v_cvt_pk_f16_f32 v110, v110, v111
	v_cvt_pk_f16_f32 v111, v112, v113
	s_waitcnt vmcnt(17)
	v_cvt_pk_f16_f32 v112, v102, v103
	v_cvt_pk_f16_f32 v113, v104, v105
	s_waitcnt vmcnt(16)
	v_cvt_pk_f16_f32 v86, v86, v87
	v_cvt_pk_f16_f32 v87, v88, v89
	v_mfma_f32_16x16x32_f16 v[102:105], v[30:33], v[110:113], 0
	s_waitcnt vmcnt(15)
	v_cvt_pk_f16_f32 v88, v82, v83
	v_cvt_pk_f16_f32 v89, v84, v85
	s_waitcnt vmcnt(13)
	v_cvt_pk_f16_f32 v82, v142, v143
	v_mfma_f32_16x16x32_f16 v[162:165], v[46:49], v[110:113], 0
	v_cvt_pk_f16_f32 v83, v144, v145
	s_waitcnt vmcnt(12)
	v_cvt_pk_f16_f32 v84, v138, v139
	v_cvt_pk_f16_f32 v85, v140, v141
	v_mfma_f32_16x16x32_f16 v[166:169], v[54:57], v[110:113], 0
	s_waitcnt vmcnt(11)
	v_cvt_pk_f16_f32 v134, v134, v135
	v_cvt_pk_f16_f32 v135, v136, v137
	s_waitcnt vmcnt(10)
	v_cvt_pk_f16_f32 v136, v130, v131
	v_mfma_f32_16x16x32_f16 v[102:105], v[22:25], v[86:89], v[102:105]
	v_cvt_pk_f16_f32 v137, v132, v133
	s_add_i32 s24, s36, 4
	s_add_i32 s25, s24, s40
	v_mfma_f32_16x16x32_f16 v[170:173], v[62:65], v[110:113], 0
	v_mfma_f32_16x16x32_f16 v[138:141], v[34:37], v[86:89], v[162:165]
	v_mfma_f32_16x16x32_f16 v[142:145], v[50:53], v[86:89], v[166:169]
	s_nop 1
	v_cndmask_b32_e64 v162, v137, v85, s[10:11]
	v_cndmask_b32_e64 v163, v136, v84, s[10:11]
	v_cndmask_b32_e64 v164, v135, v83, s[10:11]
	v_mfma_f32_16x16x32_f16 v[102:105], v[18:21], v[82:85], v[102:105]
	v_cndmask_b32_e64 v165, v134, v82, s[10:11]
	v_cndmask_b32_e64 v165, v165, v86, s[8:9]
	v_cndmask_b32_e64 v164, v164, v87, s[8:9]
	v_mfma_f32_16x16x32_f16 v[130:133], v[58:61], v[86:89], v[170:173]
	v_cndmask_b32_e64 v163, v163, v88, s[8:9]
	v_cndmask_b32_e64 v162, v162, v89, s[8:9]
	v_cndmask_b32_e64 v113, v162, v113, s[4:5]
	v_mfma_f32_16x16x32_f16 v[86:89], v[26:29], v[82:85], v[138:141]
	v_cndmask_b32_e64 v112, v163, v112, s[4:5]
	v_cndmask_b32_e64 v111, v164, v111, s[4:5]
	v_cndmask_b32_e64 v110, v165, v110, s[4:5]
	v_mfma_f32_16x16x32_f16 v[138:141], v[38:41], v[82:85], v[142:145]
	s_nop 2
	v_lshl_or_b32 v142, s25, 8, v1
	v_mfma_f32_16x16x32_f16 v[102:105], v[14:17], v[134:137], v[102:105]
	v_mfma_f32_16x16x32_f16 v[82:85], v[42:45], v[82:85], v[130:133]
	s_nop 2
	v_or_b32_e32 v130, s38, v142
	v_ashrrev_i32_e32 v131, 31, v130
	v_lshl_add_u64 v[130:131], v[130:131], 4, s[20:21]
	v_mfma_f32_16x16x32_f16 v[86:89], v[2:5], v[134:137], v[86:89]
	global_store_dwordx4 v[130:131], v[110:113], off sc0 sc1 nt
	s_nop 1
	v_max_f32_e32 v110, v103, v103
	v_max_f32_e32 v111, v102, v102
	v_max_f32_e32 v110, v111, v110
	v_max3_f32 v110, v110, v104, v105
	s_nop 0
	v_max3_f32 v130, v110, v86, v87
	v_mfma_f32_16x16x32_f16 v[110:113], v[6:9], v[134:137], v[138:141]
	v_max3_f32 v130, v130, v88, v89
	s_nop 6
	v_max3_f32 v130, v130, v110, v111
	v_max3_f32 v138, v130, v112, v113
	v_mfma_f32_16x16x32_f16 v[130:133], v[10:13], v[134:137], v[82:85]
	s_nop 7
	v_max3_f32 v82, v138, v130, v131
	v_max3_f32 v82, v82, v132, v133
	v_mov_b32_e32 v83, v82
	s_nop 1
	v_permlane16_swap_b32_e32 v82, v83
	v_max_f32_e32 v83, v83, v83
	v_max_f32_e32 v82, v82, v82
	v_max_f32_e32 v82, v82, v83
	v_mov_b32_e32 v83, v82
	s_nop 1
	v_permlane32_swap_b32_e32 v82, v83
	v_max_f32_e32 v83, v83, v83
	v_max_f32_e32 v82, v82, v82
	v_max_f32_e32 v82, v82, v83
	v_mul_f32_e32 v134, 0xbfb8aa3b, v82
	v_fmamk_f32 v82, v102, 0x3fb8aa3b, v134
	v_exp_f32_e32 v82, v82
	v_fmamk_f32 v83, v103, 0x3fb8aa3b, v134
	v_exp_f32_e32 v83, v83
	v_fmamk_f32 v84, v104, 0x3fb8aa3b, v134
	v_exp_f32_e32 v84, v84
	v_fmamk_f32 v85, v105, 0x3fb8aa3b, v134
	v_exp_f32_e32 v85, v85
	v_fmamk_f32 v86, v86, 0x3fb8aa3b, v134
	v_add_f32_e32 v102, 0, v82
	v_exp_f32_e32 v86, v86
	v_fmamk_f32 v87, v87, 0x3fb8aa3b, v134
	v_add_f32_e32 v102, v83, v102
	v_exp_f32_e32 v87, v87
	v_fmamk_f32 v88, v88, 0x3fb8aa3b, v134
	v_add_f32_e32 v102, v84, v102
	v_exp_f32_e32 v88, v88
	v_fmamk_f32 v89, v89, 0x3fb8aa3b, v134
	v_add_f32_e32 v102, v85, v102
	v_exp_f32_e32 v89, v89
	v_add_f32_e32 v102, v86, v102
	v_add_f32_e32 v102, v87, v102
	v_add_f32_e32 v102, v88, v102
	v_add_f32_e32 v135, v89, v102
	v_fmamk_f32 v102, v110, 0x3fb8aa3b, v134
	v_exp_f32_e32 v102, v102
	v_fmamk_f32 v103, v111, 0x3fb8aa3b, v134
	v_exp_f32_e32 v103, v103
	v_fmamk_f32 v104, v112, 0x3fb8aa3b, v134
	v_exp_f32_e32 v104, v104
	v_fmamk_f32 v105, v113, 0x3fb8aa3b, v134
	v_exp_f32_e32 v105, v105
	v_add_f32_e32 v110, v102, v135
	v_add_f32_e32 v110, v103, v110
	v_add_f32_e32 v110, v104, v110
	v_add_f32_e32 v135, v105, v110
	v_fmamk_f32 v110, v130, 0x3fb8aa3b, v134
	v_exp_f32_e32 v110, v110
	v_fmamk_f32 v111, v131, 0x3fb8aa3b, v134
	v_exp_f32_e32 v111, v111
	v_fmamk_f32 v112, v132, 0x3fb8aa3b, v134
	v_exp_f32_e32 v112, v112
	v_fmac_f32_e32 v134, 0x3fb8aa3b, v133
	v_exp_f32_e32 v113, v134
	v_add_f32_e32 v130, v110, v135
	v_add_f32_e32 v130, v111, v130
	v_add_f32_e32 v130, v112, v130
	v_add_f32_e32 v131, v113, v130
	v_mov_b32_e32 v132, v131
	s_nop 1
	v_permlane16_swap_b32_e32 v131, v132
	v_add_f32_e32 v131, v131, v132
	v_lshl_or_b32 v130, s24, 4, v199
	v_mov_b32_e32 v132, v131
	s_movk_i32 s24, 0xc8
	s_nop 0
	v_permlane32_swap_b32_e32 v131, v132
	v_cmp_gt_u32_e32 vcc, s24, v130
	s_and_saveexec_b64 s[24:25], vcc
	s_cbranch_execz .LBB0_110
	v_add_f32_e32 v131, v131, v132
	v_rcp_f32_e32 v132, v131
	v_lshl_add_u32 v130, v130, 3, v186
	v_pk_mul_f32 v[82:83], v[132:133], v[82:83] op_sel_hi:[0,1]
	v_pk_mul_f32 v[84:85], v[132:133], v[84:85] op_sel_hi:[0,1]
	v_cvt_pk_f16_f32 v82, v82, v83
	v_cvt_pk_f16_f32 v83, v84, v85
	ds_write_b64 v130, v[82:83]
	v_pk_mul_f32 v[82:83], v[132:133], v[86:87] op_sel_hi:[0,1]
	v_pk_mul_f32 v[84:85], v[132:133], v[88:89] op_sel_hi:[0,1]
	v_cvt_pk_f16_f32 v82, v82, v83
	v_cvt_pk_f16_f32 v83, v84, v85
	ds_write_b64 v130, v[82:83] offset:6464
	v_pk_mul_f32 v[82:83], v[132:133], v[102:103] op_sel_hi:[0,1]
	v_pk_mul_f32 v[84:85], v[132:133], v[104:105] op_sel_hi:[0,1]
	v_cvt_pk_f16_f32 v82, v82, v83
	v_cvt_pk_f16_f32 v83, v84, v85
	ds_write_b64 v130, v[82:83] offset:12928
	v_pk_mul_f32 v[82:83], v[132:133], v[110:111] op_sel_hi:[0,1]
	v_pk_mul_f32 v[84:85], v[132:133], v[112:113] op_sel_hi:[0,1]
	v_cvt_pk_f16_f32 v82, v82, v83
	v_cvt_pk_f16_f32 v83, v84, v85
	ds_write_b64 v130, v[82:83] offset:19392

.LBB0_113:
	s_waitcnt vmcnt(9)
	v_cvt_pk_f16_f32 v82, v122, v123
	v_cvt_pk_f16_f32 v83, v124, v125
	s_waitcnt vmcnt(8)
	v_cvt_pk_f16_f32 v84, v118, v119
	v_cvt_pk_f16_f32 v85, v120, v121
	s_waitcnt vmcnt(7)
	v_cvt_pk_f16_f32 v94, v94, v95
	v_cvt_pk_f16_f32 v95, v96, v97
	v_mfma_f32_16x16x32_f16 v[86:89], v[30:33], v[82:85], 0
	s_waitcnt vmcnt(6)
	v_cvt_pk_f16_f32 v96, v90, v91
	v_cvt_pk_f16_f32 v97, v92, v93
	s_waitcnt vmcnt(4)
	v_cvt_pk_f16_f32 v90, v158, v159
	v_mfma_f32_16x16x32_f16 v[102:105], v[46:49], v[82:85], 0
	v_cvt_pk_f16_f32 v91, v160, v161
	s_waitcnt vmcnt(3)
	v_cvt_pk_f16_f32 v92, v154, v155
	v_cvt_pk_f16_f32 v93, v156, v157
	v_mfma_f32_16x16x32_f16 v[110:113], v[54:57], v[82:85], 0
	s_waitcnt vmcnt(2)
	v_cvt_pk_f16_f32 v122, v150, v151
	v_cvt_pk_f16_f32 v123, v152, v153
	s_waitcnt vmcnt(1)
	v_cvt_pk_f16_f32 v124, v146, v147
	v_mfma_f32_16x16x32_f16 v[86:89], v[22:25], v[94:97], v[86:89]
	v_cvt_pk_f16_f32 v125, v148, v149
	v_cndmask_b32_e64 v130, v125, v93, s[10:11]
	v_cndmask_b32_e64 v131, v124, v92, s[10:11]
	v_mfma_f32_16x16x32_f16 v[118:121], v[62:65], v[82:85], 0
	v_cndmask_b32_e64 v132, v123, v91, s[10:11]
	v_cndmask_b32_e64 v133, v122, v90, s[10:11]
	s_add_i32 s24, s36, 6
	v_mfma_f32_16x16x32_f16 v[102:105], v[34:37], v[94:97], v[102:105]
	v_cndmask_b32_e64 v133, v133, v94, s[8:9]
	v_cndmask_b32_e64 v132, v132, v95, s[8:9]
	v_cndmask_b32_e64 v131, v131, v96, s[8:9]
	v_mfma_f32_16x16x32_f16 v[110:113], v[50:53], v[94:97], v[110:113]
	v_cndmask_b32_e64 v130, v130, v97, s[8:9]
	v_cndmask_b32_e64 v85, v130, v85, s[4:5]
	v_cndmask_b32_e64 v84, v131, v84, s[4:5]
	v_mfma_f32_16x16x32_f16 v[86:89], v[18:21], v[90:93], v[86:89]
	v_cndmask_b32_e64 v83, v132, v83, s[4:5]
	v_cndmask_b32_e64 v82, v133, v82, s[4:5]
	s_add_i32 s4, s24, s40
	v_mfma_f32_16x16x32_f16 v[118:121], v[58:61], v[94:97], v[118:121]
	v_mfma_f32_16x16x32_f16 v[94:97], v[26:29], v[90:93], v[102:105]
	v_mfma_f32_16x16x32_f16 v[102:105], v[38:41], v[90:93], v[110:113]
	s_nop 2
	v_lshl_or_b32 v110, s4, 8, v1
	v_mfma_f32_16x16x32_f16 v[86:89], v[14:17], v[122:125], v[86:89]
	v_or_b32_e32 v110, s38, v110
	v_ashrrev_i32_e32 v111, 31, v110
	v_lshl_add_u64 v[110:111], v[110:111], 4, s[20:21]
	v_mfma_f32_16x16x32_f16 v[90:93], v[42:45], v[90:93], v[118:121]
	global_store_dwordx4 v[110:111], v[82:85], off sc0 sc1 nt
	s_movk_i32 s4, 0xc8
	v_mfma_f32_16x16x32_f16 v[94:97], v[2:5], v[122:125], v[94:97]
	s_nop 0
	v_max_f32_e32 v82, v87, v87
	v_max_f32_e32 v83, v86, v86
	v_max_f32_e32 v82, v83, v82
	v_mfma_f32_16x16x32_f16 v[102:105], v[6:9], v[122:125], v[102:105]
	v_max3_f32 v82, v82, v88, v89
	s_nop 1
	v_max3_f32 v82, v82, v94, v95
	v_max3_f32 v82, v82, v96, v97
	v_mfma_f32_16x16x32_f16 v[110:113], v[10:13], v[122:125], v[90:93]
	s_nop 1
	v_max3_f32 v82, v82, v102, v103
	v_max3_f32 v82, v82, v104, v105
	s_nop 3
	v_max3_f32 v82, v82, v110, v111
	v_max3_f32 v82, v82, v112, v113
	v_mov_b32_e32 v83, v82
	s_nop 1
	v_permlane16_swap_b32_e32 v82, v83
	v_max_f32_e32 v83, v83, v83
	v_max_f32_e32 v82, v82, v82
	v_max_f32_e32 v82, v82, v83
	v_mov_b32_e32 v83, v82
	s_nop 1
	v_permlane32_swap_b32_e32 v82, v83
	v_max_f32_e32 v83, v83, v83
	v_max_f32_e32 v82, v82, v82
	v_max_f32_e32 v82, v82, v83
	v_mul_f32_e32 v118, 0xbfb8aa3b, v82
	v_fmamk_f32 v82, v86, 0x3fb8aa3b, v118
	v_exp_f32_e32 v82, v82
	v_fmamk_f32 v83, v87, 0x3fb8aa3b, v118
	v_exp_f32_e32 v83, v83
	v_fmamk_f32 v84, v88, 0x3fb8aa3b, v118
	v_exp_f32_e32 v84, v84
	v_fmamk_f32 v85, v89, 0x3fb8aa3b, v118
	v_exp_f32_e32 v85, v85
	v_add_f32_e32 v86, 0, v82
	v_add_f32_e32 v86, v83, v86
	v_add_f32_e32 v86, v84, v86
	v_add_f32_e32 v90, v85, v86
	v_fmamk_f32 v86, v94, 0x3fb8aa3b, v118
	v_exp_f32_e32 v86, v86
	v_fmamk_f32 v87, v95, 0x3fb8aa3b, v118
	v_exp_f32_e32 v87, v87
	v_fmamk_f32 v88, v96, 0x3fb8aa3b, v118
	v_exp_f32_e32 v88, v88
	v_fmamk_f32 v89, v97, 0x3fb8aa3b, v118
	v_exp_f32_e32 v89, v89
	v_add_f32_e32 v90, v86, v90
	v_add_f32_e32 v90, v87, v90
	v_add_f32_e32 v90, v88, v90
	v_add_f32_e32 v94, v89, v90
	v_fmamk_f32 v90, v102, 0x3fb8aa3b, v118
	v_exp_f32_e32 v90, v90
	v_fmamk_f32 v91, v103, 0x3fb8aa3b, v118
	v_exp_f32_e32 v91, v91
	v_fmamk_f32 v92, v104, 0x3fb8aa3b, v118
	v_exp_f32_e32 v92, v92
	v_fmamk_f32 v93, v105, 0x3fb8aa3b, v118
	v_exp_f32_e32 v93, v93
	v_add_f32_e32 v94, v90, v94
	v_add_f32_e32 v94, v91, v94
	v_add_f32_e32 v94, v92, v94
	v_add_f32_e32 v102, v93, v94
	v_fmamk_f32 v94, v110, 0x3fb8aa3b, v118
	v_exp_f32_e32 v94, v94
	v_fmamk_f32 v95, v111, 0x3fb8aa3b, v118
	v_exp_f32_e32 v95, v95
	v_fmamk_f32 v96, v112, 0x3fb8aa3b, v118
	v_exp_f32_e32 v96, v96
	v_fmac_f32_e32 v118, 0x3fb8aa3b, v113
	v_exp_f32_e32 v97, v118
	v_add_f32_e32 v102, v94, v102
	v_add_f32_e32 v102, v95, v102
	v_add_f32_e32 v102, v96, v102
	v_add_f32_e32 v103, v97, v102
	v_mov_b32_e32 v104, v103
	s_nop 1
	v_permlane16_swap_b32_e32 v103, v104
	v_add_f32_e32 v103, v103, v104
	v_lshl_or_b32 v102, s24, 4, v199
	v_mov_b32_e32 v104, v103
	s_nop 1
	v_permlane32_swap_b32_e32 v103, v104
	v_cmp_gt_u32_e32 vcc, s4, v102
	s_and_saveexec_b64 s[4:5], vcc
	s_cbranch_execz .LBB0_115
	v_add_f32_e32 v103, v103, v104
	v_rcp_f32_e32 v104, v103
	v_lshl_add_u32 v102, v102, 3, v186
	v_pk_mul_f32 v[82:83], v[104:105], v[82:83] op_sel_hi:[0,1]
	v_pk_mul_f32 v[84:85], v[104:105], v[84:85] op_sel_hi:[0,1]
	v_cvt_pk_f16_f32 v82, v82, v83
	v_cvt_pk_f16_f32 v83, v84, v85
	ds_write_b64 v102, v[82:83]
	v_pk_mul_f32 v[82:83], v[104:105], v[86:87] op_sel_hi:[0,1]
	v_pk_mul_f32 v[84:85], v[104:105], v[88:89] op_sel_hi:[0,1]
	v_cvt_pk_f16_f32 v82, v82, v83
	v_cvt_pk_f16_f32 v83, v84, v85
	ds_write_b64 v102, v[82:83] offset:6464
	v_pk_mul_f32 v[82:83], v[104:105], v[90:91] op_sel_hi:[0,1]
	v_pk_mul_f32 v[84:85], v[104:105], v[92:93] op_sel_hi:[0,1]
	v_cvt_pk_f16_f32 v82, v82, v83
	v_cvt_pk_f16_f32 v83, v84, v85
	ds_write_b64 v102, v[82:83] offset:12928
	v_pk_mul_f32 v[82:83], v[104:105], v[94:95] op_sel_hi:[0,1]
	v_pk_mul_f32 v[84:85], v[104:105], v[96:97] op_sel_hi:[0,1]
	v_cvt_pk_f16_f32 v82, v82, v83
	v_cvt_pk_f16_f32 v83, v84, v85
	ds_write_b64 v102, v[82:83] offset:19392

.LBB0_120:
	v_mfma_f32_16x16x32_f16 v[30:33], v[30:33], v[82:85], 0
	s_mul_i32 s4, s3, 0xd00
	s_addk_i32 s4, 0xc00
	v_mfma_f32_16x16x32_f16 v[46:49], v[46:49], v[82:85], 0
	v_mfma_f32_16x16x32_f16 v[54:57], v[54:57], v[82:85], 0
	v_mfma_f32_16x16x32_f16 v[22:25], v[22:25], v[86:89], v[30:33]
	v_mfma_f32_16x16x32_f16 v[62:65], v[62:65], v[82:85], 0
	v_mfma_f32_16x16x32_f16 v[30:33], v[34:37], v[86:89], v[46:49]
	v_mfma_f32_16x16x32_f16 v[34:37], v[50:53], v[86:89], v[54:57]
	v_mfma_f32_16x16x32_f16 v[18:21], v[18:21], v[90:93], v[22:25]
	v_mfma_f32_16x16x32_f16 v[46:49], v[58:61], v[86:89], v[62:65]
	v_mfma_f32_16x16x32_f16 v[22:25], v[26:29], v[90:93], v[30:33]
	v_mfma_f32_16x16x32_f16 v[26:29], v[38:41], v[90:93], v[34:37]
	s_nop 3
	v_or_b32_e32 v34, s4, v1
	v_mfma_f32_16x16x32_f16 v[14:17], v[14:17], v[66:69], v[18:21]
	v_or_b32_e32 v34, s38, v34
	v_ashrrev_i32_e32 v35, 31, v34
	v_lshl_add_u64 v[34:35], v[34:35], 4, s[20:21]
	v_mfma_f32_16x16x32_f16 v[30:33], v[42:45], v[90:93], v[46:49]
	global_store_dwordx4 v[34:35], v[70:73], off sc0 sc1 nt
	s_nop 2
	v_max_f32_e32 v34, v15, v15
	v_max_f32_e32 v35, v14, v14
	v_mfma_f32_16x16x32_f16 v[18:21], v[2:5], v[66:69], v[22:25]
	v_max_f32_e32 v2, v35, v34
	v_max3_f32 v2, v2, v16, v17
	s_movk_i32 s4, 0xc8
	v_mfma_f32_16x16x32_f16 v[22:25], v[6:9], v[66:69], v[26:29]
	v_mfma_f32_16x16x32_f16 v[26:29], v[10:13], v[66:69], v[30:33]
	s_nop 2
	v_max3_f32 v2, v2, v18, v19
	v_max3_f32 v2, v2, v20, v21
	s_nop 1
	v_max3_f32 v2, v2, v22, v23
	v_max3_f32 v2, v2, v24, v25
	v_max3_f32 v2, v2, v26, v27
	v_max3_f32 v2, v2, v28, v29
	v_mov_b32_e32 v3, v2
	s_nop 1
	v_permlane16_swap_b32_e32 v2, v3
	v_max_f32_e32 v3, v3, v3
	v_max_f32_e32 v2, v2, v2
	v_max_f32_e32 v2, v2, v3
	v_mov_b32_e32 v3, v2
	s_nop 1
	v_permlane32_swap_b32_e32 v2, v3
	v_max_f32_e32 v3, v3, v3
	v_max_f32_e32 v2, v2, v2
	v_max_f32_e32 v2, v2, v3
	v_mul_f32_e32 v30, 0xbfb8aa3b, v2
	v_fmamk_f32 v2, v14, 0x3fb8aa3b, v30
	v_exp_f32_e32 v2, v2
	v_fmamk_f32 v3, v15, 0x3fb8aa3b, v30
	v_exp_f32_e32 v3, v3
	v_fmamk_f32 v4, v16, 0x3fb8aa3b, v30
	v_exp_f32_e32 v4, v4
	v_fmamk_f32 v5, v17, 0x3fb8aa3b, v30
	v_exp_f32_e32 v5, v5
	v_add_f32_e32 v6, 0, v2
	v_add_f32_e32 v6, v3, v6
	v_add_f32_e32 v6, v4, v6
	v_add_f32_e32 v10, v5, v6
	v_fmamk_f32 v6, v18, 0x3fb8aa3b, v30
	v_exp_f32_e32 v6, v6
	v_fmamk_f32 v7, v19, 0x3fb8aa3b, v30
	v_exp_f32_e32 v7, v7
	v_fmamk_f32 v8, v20, 0x3fb8aa3b, v30
	v_exp_f32_e32 v8, v8
	v_fmamk_f32 v9, v21, 0x3fb8aa3b, v30
	v_exp_f32_e32 v9, v9
	v_add_f32_e32 v10, v6, v10
	v_add_f32_e32 v10, v7, v10
	v_add_f32_e32 v10, v8, v10
	v_add_f32_e32 v14, v9, v10
	v_fmamk_f32 v10, v22, 0x3fb8aa3b, v30
	v_exp_f32_e32 v10, v10
	v_fmamk_f32 v11, v23, 0x3fb8aa3b, v30
	v_exp_f32_e32 v11, v11
	v_fmamk_f32 v12, v24, 0x3fb8aa3b, v30
	v_exp_f32_e32 v12, v12
	v_fmamk_f32 v13, v25, 0x3fb8aa3b, v30
	v_exp_f32_e32 v13, v13
	v_add_f32_e32 v14, v10, v14
	v_add_f32_e32 v14, v11, v14
	v_add_f32_e32 v14, v12, v14
	v_add_f32_e32 v18, v13, v14
	v_fmamk_f32 v14, v26, 0x3fb8aa3b, v30
	v_exp_f32_e32 v14, v14
	v_fmamk_f32 v15, v27, 0x3fb8aa3b, v30
	v_exp_f32_e32 v15, v15
	v_fmamk_f32 v16, v28, 0x3fb8aa3b, v30
	v_exp_f32_e32 v16, v16
	v_fmac_f32_e32 v30, 0x3fb8aa3b, v29
	v_exp_f32_e32 v17, v30
	v_add_f32_e32 v18, v14, v18
	v_add_f32_e32 v18, v15, v18
	v_add_f32_e32 v18, v16, v18
	v_add_f32_e32 v19, v17, v18
	v_mov_b32_e32 v20, v19
	s_nop 1
	v_permlane16_swap_b32_e32 v19, v20
	v_add_f32_e32 v19, v19, v20
	v_or_b32_e32 v18, 0xc0, v199
	v_mov_b32_e32 v20, v19
	s_nop 1
	v_permlane32_swap_b32_e32 v19, v20
	v_cmp_gt_u32_e32 vcc, s4, v18
	s_and_saveexec_b64 s[4:5], vcc
	s_cbranch_execz .LBB0_122
	v_add_f32_e32 v19, v19, v20
	v_rcp_f32_e32 v20, v19
	v_lshl_add_u32 v18, v18, 3, v186
	v_pk_mul_f32 v[2:3], v[20:21], v[2:3] op_sel_hi:[0,1]
	v_pk_mul_f32 v[4:5], v[20:21], v[4:5] op_sel_hi:[0,1]
	v_cvt_pk_f16_f32 v2, v2, v3
	v_cvt_pk_f16_f32 v3, v4, v5
	ds_write_b64 v18, v[2:3]
	v_pk_mul_f32 v[2:3], v[20:21], v[6:7] op_sel_hi:[0,1]
	v_pk_mul_f32 v[4:5], v[20:21], v[8:9] op_sel_hi:[0,1]
	v_cvt_pk_f16_f32 v2, v2, v3
	v_cvt_pk_f16_f32 v3, v4, v5
	ds_write_b64 v18, v[2:3] offset:6464
	v_pk_mul_f32 v[2:3], v[20:21], v[10:11] op_sel_hi:[0,1]
	v_pk_mul_f32 v[4:5], v[20:21], v[12:13] op_sel_hi:[0,1]
	v_cvt_pk_f16_f32 v2, v2, v3
	v_cvt_pk_f16_f32 v3, v4, v5
	ds_write_b64 v18, v[2:3] offset:12928
	v_pk_mul_f32 v[2:3], v[20:21], v[14:15] op_sel_hi:[0,1]
	v_pk_mul_f32 v[4:5], v[20:21], v[16:17] op_sel_hi:[0,1]
	v_cvt_pk_f16_f32 v2, v2, v3
	v_cvt_pk_f16_f32 v3, v4, v5
	ds_write_b64 v18, v[2:3] offset:19392
